# pending-barrier poll loops bounded like every other hand-written poll (no functional or timing change intended)
# speedup vs baseline: 1.0042x; 1.0042x over previous
.Lmodfin_end:
	s_mov_b64 exec, -1
	v_readlane_b32 s98, v238, 0
	s_waitcnt vmcnt(0)
	s_waitcnt lgkmcnt(0)
	s_barrier
	s_mov_b64 s[0:1], exec
	v_readlane_b32 s2, v235, 5
	v_readlane_b32 s3, v235, 6
	s_and_b64 s[2:3], s[0:1], s[2:3]
	s_xor_b64 s[0:1], s[2:3], s[0:1]
	s_mov_b64 exec, s[2:3]
	s_cbranch_execz .LBB0_208
	s_cmp_eq_u32 s98, 0
	s_cbranch_scc1 .Lxb_nopend_1
	v_readlane_b32 s100, v235, 7
	v_readlane_b32 s101, v235, 8
	v_mov_b32_e32 v237, 0x3400
	v_mov_b32_e32 v239, 0
	s_nop 3
.Lxb_pend_1:
	global_load_dword v238, v237, s[100:101] sc1
	s_waitcnt vmcnt(0)
	v_cmp_le_u32_e32 vcc, s98, v238
	s_cbranch_vccnz .Lxb_pendok_1
	s_sleep 1
	v_add_u32_e32 v239, 1, v239
	v_cmp_gt_u32_e32 vcc, 0x8000, v239
	s_cbranch_vccnz .Lxb_pend_1

.LBB0_293:
	s_waitcnt vmcnt(0)
	s_waitcnt vmcnt(0)
	s_barrier
	s_mov_b64 s[0:1], exec
	v_readlane_b32 s2, v235, 5
	v_readlane_b32 s3, v235, 6
	s_and_b64 s[2:3], s[0:1], s[2:3]
	s_xor_b64 s[0:1], s[2:3], s[0:1]
	s_mov_b64 exec, s[2:3]
	s_cbranch_execz .LBB0_346
	s_cmp_eq_u32 s98, 0
	s_cbranch_scc1 .Lxb_nopend_2
	v_readlane_b32 s100, v235, 7
	v_readlane_b32 s101, v235, 8
	v_mov_b32_e32 v237, 0x3400
	v_mov_b32_e32 v239, 0
	s_nop 3

.LBB0_373:
	s_waitcnt lgkmcnt(0)
	s_barrier
	s_waitcnt vmcnt(0)
	s_barrier
	s_mov_b64 s[0:1], exec
	v_readlane_b32 s2, v235, 5
	v_readlane_b32 s3, v235, 6
	s_and_b64 s[2:3], s[0:1], s[2:3]
	s_xor_b64 s[0:1], s[2:3], s[0:1]
	s_mov_b64 exec, s[2:3]
	s_cbranch_execz .LBB0_426
	s_cmp_eq_u32 s98, 0
	s_cbranch_scc1 .Lxb_nopend_3
	v_readlane_b32 s100, v235, 7
	v_readlane_b32 s101, v235, 8
	v_mov_b32_e32 v237, 0x3400
	v_mov_b32_e32 v239, 0
	s_nop 3

.LBB0_499:
	s_waitcnt vmcnt(0)
	s_waitcnt lgkmcnt(0)
	s_barrier
	s_mov_b64 s[0:1], exec
	v_readlane_b32 s2, v235, 5
	v_readlane_b32 s3, v235, 6
	s_and_b64 s[2:3], s[0:1], s[2:3]
	s_xor_b64 s[0:1], s[2:3], s[0:1]
	s_mov_b64 exec, s[2:3]
	s_cbranch_execz .LBB0_553
	s_cmp_eq_u32 s98, 0
	s_cbranch_scc1 .Lxb_nopend_5
	v_readlane_b32 s100, v235, 7
	v_readlane_b32 s101, v235, 8
	v_mov_b32_e32 v237, 0x3400
	v_mov_b32_e32 v239, 0
	s_nop 3

.LBB0_573:
	s_waitcnt vmcnt(0)
	s_barrier
	s_mov_b64 s[0:1], exec
	v_readlane_b32 s2, v235, 5
	v_readlane_b32 s3, v235, 6
	s_and_b64 s[2:3], s[0:1], s[2:3]
	s_xor_b64 s[0:1], s[2:3], s[0:1]
	s_mov_b64 exec, s[2:3]
	s_cbranch_execz .LBB0_626
	s_cmp_eq_u32 s98, 0
	s_cbranch_scc1 .Lxb_nopend_6
	v_readlane_b32 s100, v235, 7
	v_readlane_b32 s101, v235, 8
	v_mov_b32_e32 v237, 0x3400
	v_mov_b32_e32 v239, 0
	s_nop 3

.LBB0_919:
	s_waitcnt vmcnt(0)
	s_waitcnt vmcnt(63) expcnt(7) lgkmcnt(15)
	s_barrier
	s_mov_b64 s[0:1], exec
	v_readlane_b32 s2, v235, 5
	v_readlane_b32 s3, v235, 6
	s_and_b64 s[2:3], s[0:1], s[2:3]
	s_xor_b64 s[0:1], s[2:3], s[0:1]
	s_mov_b64 exec, s[2:3]
	s_cbranch_execz .LBB0_972
	s_cmp_eq_u32 s98, 0
	s_cbranch_scc1 .Lxb_nopend_8
	v_readlane_b32 s100, v235, 7
	v_readlane_b32 s101, v235, 8
	v_mov_b32_e32 v237, 0x3400
	v_mov_b32_e32 v239, 0
	s_nop 3

.LBB0_976:
	s_or_b64 exec, exec, s[2:3]
	s_waitcnt vmcnt(0)
	s_barrier
	s_mov_b64 s[2:3], exec
	v_readlane_b32 s4, v235, 5
	v_readlane_b32 s5, v235, 6
	s_and_b64 s[4:5], s[2:3], s[4:5]
	s_xor_b64 s[2:3], s[4:5], s[2:3]
	s_mov_b64 exec, s[4:5]
	s_cbranch_execz .LBB0_1029
	s_cmp_eq_u32 s98, 0
	s_cbranch_scc1 .Lxb_nopend_9
	v_readlane_b32 s100, v235, 7
	v_readlane_b32 s101, v235, 8
	v_mov_b32_e32 v237, 0x3400
	v_mov_b32_e32 v239, 0
	s_nop 3

.LBB0_1115:
	s_waitcnt vmcnt(0)
	s_waitcnt vmcnt(0) lgkmcnt(0)
	s_barrier
	s_mov_b64 s[0:1], exec
	v_readlane_b32 s2, v235, 5
	v_readlane_b32 s3, v235, 6
	s_and_b64 s[2:3], s[0:1], s[2:3]
	s_xor_b64 s[0:1], s[2:3], s[0:1]
	s_mov_b64 exec, s[2:3]
	s_cbranch_execz .LBB0_1168
	s_cmp_eq_u32 s98, 0
	s_cbranch_scc1 .Lxb_nopend_10
	v_readlane_b32 s100, v235, 7
	v_readlane_b32 s101, v235, 8
	v_mov_b32_e32 v237, 0x3400
	v_mov_b32_e32 v239, 0
	s_nop 3

.Lx1_none:
	s_mov_b64 s[0:1], exec
	v_readlane_b32 s2, v235, 5
	v_readlane_b32 s3, v235, 6
	s_and_b64 s[2:3], s[0:1], s[2:3]
	v_readlane_b32 s46, v235, 14
	s_xor_b64 s[0:1], s[2:3], s[0:1]
	v_readlane_b32 s47, v235, 15
	s_mov_b64 exec, s[2:3]
	s_cbranch_execz .LBB0_1241
	s_cmp_eq_u32 s98, 0
	s_cbranch_scc1 .Lxb_nopend_11
	v_readlane_b32 s100, v235, 7
	v_readlane_b32 s101, v235, 8
	v_mov_b32_e32 v237, 0x3400
	v_mov_b32_e32 v239, 0
	s_nop 3
